# v73 without the static priority raise of waves 4-7 in the differential-attention units
# speedup vs baseline: 1.0088x; 1.0088x over previous
; DI void attn_unit_d8(unsigned char* lds, const AttnArgs& a) {
;     int tid = threadIdx.x; asm volatile("" : "+v"(tid));
;     const int lane = tid & 63, r = lane & 31, h = lane >> 5; const int wid = __builtin_amdgcn_readfirstlane(tid >> 6);
;     v8i qfa, qfb;
;     { const bf16_t* qp = a.q + (size_t)(wid * 32 + r) * 256 + 32 * h;
;       const u32x4 q0 = *(const u32x4*)qp, q1 = *(const u32x4*)(qp + 8), q2 = *(const u32x4*)(qp + 16), q3 = *(const u32x4*)(qp + 24);
;       const u32x2 c0 = bf8_to_fp8(q0), c1 = bf8_to_fp8(q1), c2 = bf8_to_fp8(q2), c3 = bf8_to_fp8(q3);
;       const v8i qv = (v8i){(int)c0.x, (int)c0.y, (int)c1.x, (int)c1.y, (int)c2.x, (int)c2.y, (int)c3.x, (int)c3.y}, zz = (v8i){0, 0, 0, 0, 0, 0, 0, 0};
;       qfa = h == 0 ? qv : zz; qfb = h == 1 ? qv : zz; }
;     const int lrow = tid >> 3, lch = tid & 7;
;     const unsigned char* vsrc = a.vt8 + (size_t)lrow * KEYS + 8 * lch;
;     const int ldst = lrow * A8_PITCH + lch * 8;
;     const int ldv = A8_VOFF + lrow * A8_PITCH + (lch >> 2) * 16 + (lch & 3) * 4;
;     const int koff = r * A8_PITCH + 32 * h, voff = A8_VOFF + r * A8_PITCH + 32 * h;
;     f32x16 o0[2], o1[2];
; #pragma unroll
;     for (int d = 0; d < 2; ++d) { o0[d] = (f32x16){}; o1[d] = (f32x16){}; }
;     f32x4 l0 = {0.f, 0.f, 0.f, 0.f}, l1 = {0.f, 0.f, 0.f, 0.f};
;     constexpr int D8_SLOT = 2 * 64 * A8_PITCH;
;     u32x2 kreg0, vreg0, kreg1, vreg1;
;     auto gload = [&](int t, u32x2& kreg, u32x2& vreg) __attribute__((always_inline)) {
;         const unsigned char* kp = (t < 64) ? a.klat8 + (size_t)(t * 64 + lrow) * 256 : a.kctx8 + (size_t)((t - 64) * 64 + lrow) * 256;
;         kreg = *(const u32x2*)(kp + 8 * lch);
;         vreg = *(const u32x2*)(vsrc + (size_t)t * 64);
;     };
;     auto lstore = [&](int slot, const u32x2& kreg, const u32x2& vreg) __attribute__((always_inline)) { unsigned char* b = lds + slot * D8_SLOT;
;         *(u32x2*)(b + ldst) = kreg; *(unsigned*)(b + ldv) = vreg.x; *(unsigned*)(b + ldv + 32) = vreg.y; };
;     auto rd32 = [&](const unsigned char* p) __attribute__((always_inline)) -> v8i { const u32x4 lo = *(const u32x4*)p, hi = *(const u32x4*)(p + 16);
;         return (v8i){(int)lo.x, (int)lo.y, (int)lo.z, (int)lo.w, (int)hi.x, (int)hi.y, (int)hi.z, (int)hi.w}; };
;     auto expsum = [&](f32x16& sc, f32x4& l) __attribute__((always_inline)) {
; #pragma unroll
.LBB0_660:
	s_ashr_i32 s15, s14, 31
	s_lshl_b64 s[48:49], s[14:15], 9
	s_add_u32 s21, s22, s48
	s_addc_u32 s47, s23, s49
	s_lshl_b32 s19, s19, 6
	s_and_b32 s43, s19, 0xc0
	s_lshl_b32 s19, s43, 1
	s_add_u32 s52, s21, s19
	s_addc_u32 s53, s47, 0
	s_ashr_i32 s19, s18, 31
	s_ashr_i32 s21, s20, 31
	s_or_b32 s6, s43, s6
	s_lshl_b64 s[48:49], s[18:19], 8
	s_lshl_b64 s[54:55], s[20:21], 8
	s_mul_hi_i32 s19, s6, 0x1100
	s_mulk_i32 s6, 0x1100
	s_add_u32 s18, s28, s6
	s_addc_u32 s19, s29, s19
	s_add_u32 s6, s24, s48
	s_addc_u32 s21, s25, s49
	s_add_u32 s20, s6, s43
	s_addc_u32 s21, s21, 0
	s_add_u32 s6, s24, s54
	s_addc_u32 s48, s25, s55
	v_mov_b32_e32 v18, v0
	s_add_u32 s47, s6, s43
	s_addc_u32 s48, s48, 0
	v_readfirstlane_b32 s6, v18
	v_and_b32_e32 v30, 31, v18
	s_ashr_i32 s49, s6, 6
	v_lshl_or_b32 v180, s49, 5, v30
	v_ashrrev_i32_e32 v181, 31, v180
	v_bfe_u32 v214, v18, 5, 1
	v_lshlrev_b64 v[2:3], 9, v[180:181]
	v_lshl_add_u64 v[2:3], s[52:53], 0, v[2:3]
	v_lshlrev_b32_e32 v178, 6, v214
	v_lshl_add_u64 v[14:15], v[2:3], 0, v[178:179]
	global_load_dwordx4 v[2:5], v[14:15], off
	global_load_dwordx4 v[6:9], v[14:15], off offset:16
	global_load_dwordx4 v[10:13], v[14:15], off offset:32
	s_nop 0
	global_load_dwordx4 v[14:17], v[14:15], off offset:48
	s_lshl_b32 s6, s46, 6
	v_bfe_i32 v34, v18, 5, 1
	v_ashrrev_i32_e32 v215, 3, v18
	v_and_b32_e32 v35, 7, v18
	v_mov_b64_e32 v[18:19], s[18:19]
	s_add_i32 s52, s6, 0xfffff000
	v_mad_i64_i32 v[18:19], s[18:19], v215, s37, v[18:19]
	s_and_b64 s[18:19], s[16:17], exec
	s_cselect_b32 s52, s6, s52
	s_cselect_b32 s19, s21, s48
	s_cselect_b32 s18, s20, s47
	s_or_b32 s54, s6, 64
	s_add_i32 s55, s6, 0xfffff040
	v_add_u32_e32 v20, s52, v215
	s_and_b64 s[52:53], s[16:17], exec
	v_lshlrev_b32_e32 v178, 3, v35
	s_cselect_b32 s52, s54, s55
	s_or_b32 s53, s6, 0x80
	s_add_i32 s54, s6, 0xfffff080
	v_lshl_add_u64 v[182:183], v[18:19], 0, v[178:179]
	s_and_b64 s[16:17], s[16:17], exec
	v_ashrrev_i32_e32 v21, 31, v20
	v_lshl_add_u64 v[22:23], v[182:183], 0, s[6:7]
	s_cselect_b32 s6, s53, s54
	v_lshlrev_b64 v[18:19], 8, v[20:21]
	v_add_u32_e32 v20, s52, v215
	v_add_u32_e32 v24, s6, v215
	v_ashrrev_i32_e32 v21, 31, v20
	v_ashrrev_i32_e32 v25, 31, v24
	v_lshl_add_u64 v[18:19], s[18:19], 0, v[18:19]
	v_lshlrev_b64 v[20:21], 8, v[20:21]
	v_lshlrev_b64 v[24:25], 8, v[24:25]
	v_lshl_add_u64 v[18:19], v[18:19], 0, v[178:179]
	v_lshl_add_u64 v[20:21], s[18:19], 0, v[20:21]
	v_lshl_add_u64 v[24:25], s[18:19], 0, v[24:25]
	global_load_dwordx2 v[26:27], v[22:23], off
	global_load_dwordx2 v[28:29], v[22:23], off offset:64
	s_nop 0
	global_load_dwordx2 v[22:23], v[22:23], off offset:128
	s_nop 0
	global_load_dwordx2 v[18:19], v[18:19], off
	v_lshl_add_u64 v[20:21], v[20:21], 0, v[178:179]
	v_lshl_add_u64 v[24:25], v[24:25], 0, v[178:179]
	global_load_dwordx2 v[20:21], v[20:21], off
	s_nop 0
	global_load_dwordx2 v[24:25], v[24:25], off
	s_nop 0
	s_nop 0
	s_nop 0
	v_cmp_eq_u32_e32 vcc, 0, v214
	v_lshlrev_b32_e32 v36, 5, v214
	s_cmp_lt_i32 s49, 4
	s_waitcnt vmcnt(9)
	v_lshlrev_b32_e32 v37, 16, v2
	v_and_b32_e32 v2, 0xffff0000, v2
	v_lshlrev_b32_e32 v39, 16, v4
	v_and_b32_e32 v4, 0xffff0000, v4
	s_waitcnt vmcnt(8)
	v_lshlrev_b32_e32 v41, 16, v6
	v_and_b32_e32 v6, 0xffff0000, v6
	v_cvt_pk_fp8_f32 v31, v37, v2
	v_cvt_pk_fp8_f32 v32, v39, v4
	v_cvt_pk_fp8_f32 v33, v41, v6
	v_lshlrev_b32_e32 v38, 16, v3
	v_and_b32_e32 v3, 0xffff0000, v3
	v_lshlrev_b32_e32 v40, 16, v5
	v_and_b32_e32 v5, 0xffff0000, v5
	v_lshlrev_b32_e32 v42, 16, v7
	v_and_b32_e32 v7, 0xffff0000, v7
	v_lshlrev_b32_e32 v43, 16, v8
	v_and_b32_e32 v2, 0xffff0000, v8
	v_cvt_pk_fp8_f32 v31, v38, v3 op_sel:[0,0,1]
	s_nop 0
	v_cvt_pk_fp8_f32 v32, v40, v5 op_sel:[0,0,1]
	v_cvt_pk_fp8_f32 v33, v42, v7 op_sel:[0,0,1]
	v_cvt_pk_fp8_f32 v3, v43, v2
	s_waitcnt vmcnt(7)
	v_lshlrev_b32_e32 v5, 16, v10
	v_and_b32_e32 v6, 0xffff0000, v10
	s_nop 0
	v_cvt_pk_fp8_f32 v7, v5, v6
	v_lshlrev_b32_e32 v2, 16, v9
	v_and_b32_e32 v4, 0xffff0000, v9
	v_cvt_pk_fp8_f32 v3, v2, v4 op_sel:[0,0,1]
	v_lshlrev_b32_e32 v2, 16, v11
	v_and_b32_e32 v4, 0xffff0000, v11
	v_cvt_pk_fp8_f32 v7, v2, v4 op_sel:[0,0,1]
	v_lshlrev_b32_e32 v2, 16, v12
	v_and_b32_e32 v4, 0xffff0000, v12
	s_nop 0
	v_cvt_pk_fp8_f32 v5, v2, v4
	s_waitcnt vmcnt(6)
	v_lshlrev_b32_e32 v6, 16, v14
	v_and_b32_e32 v8, 0xffff0000, v14
	s_nop 0
	v_cvt_pk_fp8_f32 v9, v6, v8
	v_lshlrev_b32_e32 v8, 16, v16
	v_and_b32_e32 v10, 0xffff0000, v16
	s_nop 0
	v_cvt_pk_fp8_f32 v11, v8, v10
	v_lshlrev_b32_e32 v2, 16, v13
	v_and_b32_e32 v4, 0xffff0000, v13
	v_lshlrev_b32_e32 v6, 16, v15
	v_and_b32_e32 v8, 0xffff0000, v15
	v_cvt_pk_fp8_f32 v5, v2, v4 op_sel:[0,0,1]
	v_lshlrev_b32_e32 v4, 2, v35
	v_lshlrev_b32_e32 v10, 16, v17
	v_and_b32_e32 v12, 0xffff0000, v17
	v_cvt_pk_fp8_f32 v9, v6, v8 op_sel:[0,0,1]
	v_mul_lo_u32 v2, v215, s38
	v_and_b32_e32 v6, 16, v4
	v_cvt_pk_fp8_f32 v11, v10, v12 op_sel:[0,0,1]
	v_add_u32_e32 v216, v2, v178
	v_add_u32_e32 v2, v2, v6
	v_and_or_b32 v217, v4, 12, v2
	v_add_u32_e32 v2, 0, v217
	v_cndmask_b32_e32 v117, 0, v3, vcc
	v_mul_u32_u24_e32 v8, 0x50, v30
	v_and_b32_e32 v125, v34, v3
	v_add_u32_e32 v3, 0, v216
	v_add_u32_e32 v4, 0x1400, v2
	v_cndmask_b32_e32 v121, 0, v11, vcc
	v_cndmask_b32_e32 v120, 0, v9, vcc
	v_cndmask_b32_e32 v119, 0, v5, vcc
	v_cndmask_b32_e32 v118, 0, v7, vcc
	v_cndmask_b32_e32 v116, 0, v33, vcc
	v_cndmask_b32_e32 v115, 0, v32, vcc
	v_cndmask_b32_e32 v114, 0, v31, vcc
	v_and_b32_e32 v129, v34, v11
	v_and_b32_e32 v128, v34, v9
	v_and_b32_e32 v127, v34, v5
	v_and_b32_e32 v126, v34, v7
	v_and_b32_e32 v124, v34, v33
	v_and_b32_e32 v123, v34, v32
	v_and_b32_e32 v122, v34, v31
	s_waitcnt vmcnt(2)
	ds_write_b64 v3, v[18:19]
	ds_write2_b32 v4, v26, v27 offset1:8
	s_waitcnt vmcnt(1)
	ds_write_b64 v3, v[20:21] offset:10240
	v_add_u32_e32 v4, 0x3c00, v2
	v_add_u32_e32 v2, 0x6400, v2
	v_add3_u32 v218, v36, v8, 0
	ds_write2_b32 v4, v28, v29 offset1:8
	s_waitcnt vmcnt(0)
	ds_write_b64 v3, v[24:25] offset:20480
	ds_write2_b32 v2, v22, v23 offset1:8
	s_waitcnt lgkmcnt(0)
	s_barrier
	ds_read_b128 v[2:5], v218
	ds_read_b128 v[6:9], v218 offset:16
	s_waitcnt lgkmcnt(0)
	v_mfma_f32_32x32x64_f8f6f4 v[82:97], v[2:9], v[114:121], 0
	v_mfma_f32_32x32x64_f8f6f4 v[66:81], v[2:9], v[122:129], 0
	s_cbranch_scc1 .LBB0_662
; DI void attn_unit_d8(unsigned char* lds, const AttnArgs& a) {
;     ...
;     f32x16 o0[2], o1[2];
; #pragma unroll
;     for (int d = 0; d < 2; ++d) { o0[d] = (f32x16){}; o1[d] = (f32x16){}; }
;     f32x4 l0 = {0.f, 0.f, 0.f, 0.f}, l1 = {0.f, 0.f, 0.f, 0.f};
;     ...
;     if (wid >= 4) __builtin_amdgcn_s_setprio(1);
;     int sb = 0;
;     const v8i zz8 = (v8i){0, 0, 0, 0, 0, 0, 0, 0};
;     v8i PaX = zz8, PbX = zz8, PaY = zz8, PbY = zz8, vX0 = zz8, vX1 = zz8, vY0 = zz8, vY1 = zz8;
.LBB0_662:
	s_and_b32 s61, s42, 1
	s_lshl_b32 s61, s61, 3
	s_sub_i32 s61, 0, s61
	v_mov_b32_e32 v2, 0
	s_mov_b32 s16, 0
	v_mov_b32_e32 v138, 0
	v_mov_b32_e32 v139, 0
	v_mov_b32_e32 v140, 0
	v_mov_b32_e32 v141, 0
	v_mov_b32_e32 v142, 0
	v_mov_b32_e32 v143, 0
	v_mov_b32_e32 v144, 0
	v_mov_b32_e32 v145, 0
	v_mov_b32_e32 v130, 0
	v_mov_b32_e32 v131, 0
	v_mov_b32_e32 v132, 0
	v_mov_b32_e32 v133, 0
	v_mov_b32_e32 v134, 0
	v_mov_b32_e32 v135, 0
	v_mov_b32_e32 v136, 0
	v_mov_b32_e32 v137, 0
	v_mov_b32_e32 v154, 0
	v_mov_b32_e32 v155, 0
	v_mov_b32_e32 v156, 0
	v_mov_b32_e32 v157, 0
	v_mov_b32_e32 v158, 0
	v_mov_b32_e32 v159, 0
	v_mov_b32_e32 v160, 0
	v_mov_b32_e32 v161, 0
	v_mov_b32_e32 v146, 0
	v_mov_b32_e32 v147, 0
	v_mov_b32_e32 v148, 0
	v_mov_b32_e32 v149, 0
	v_mov_b32_e32 v150, 0
	v_mov_b32_e32 v151, 0
	v_mov_b32_e32 v152, 0
	v_mov_b32_e32 v153, 0
	v_mov_b32_e32 v3, v2
	v_mov_b32_e32 v4, v2
	v_mov_b32_e32 v5, v2
	v_mov_b32_e32 v6, v2
	v_mov_b32_e32 v7, v2
	v_mov_b32_e32 v8, v2
	v_mov_b32_e32 v9, v2
	v_mov_b32_e32 v10, v2
	v_mov_b32_e32 v11, v2
	v_mov_b32_e32 v12, v2
	v_mov_b32_e32 v13, v2
	v_mov_b32_e32 v14, v2
	v_mov_b32_e32 v15, v2
	v_mov_b32_e32 v16, v2
	v_mov_b32_e32 v17, v2
	v_mov_b32_e32 v18, v2
	v_mov_b32_e32 v19, v2
	v_mov_b32_e32 v20, v2
	v_mov_b32_e32 v21, v2
	v_mov_b32_e32 v22, v2
	v_mov_b32_e32 v23, v2
	v_mov_b32_e32 v24, v2
	v_mov_b32_e32 v25, v2
	v_mov_b32_e32 v26, v2
	v_mov_b32_e32 v27, v2
	v_mov_b32_e32 v28, v2
	v_mov_b32_e32 v29, v2
	v_mov_b32_e32 v30, v2
	v_mov_b32_e32 v31, v2
	v_mov_b32_e32 v32, v2
	v_mov_b32_e32 v33, v2
	v_mov_b32_e32 v50, v2
	v_mov_b32_e32 v51, v2
	v_mov_b32_e32 v52, v2
	v_mov_b32_e32 v53, v2
	v_mov_b32_e32 v54, v2
	v_mov_b32_e32 v55, v2
	v_mov_b32_e32 v56, v2
	v_mov_b32_e32 v57, v2
	v_mov_b32_e32 v58, v2
	v_mov_b32_e32 v59, v2
	v_mov_b32_e32 v60, v2
	v_mov_b32_e32 v61, v2
	v_mov_b32_e32 v62, v2
	v_mov_b32_e32 v63, v2
	v_mov_b32_e32 v64, v2
	v_mov_b32_e32 v65, v2
	v_mov_b32_e32 v34, v2
	v_mov_b32_e32 v35, v2
	v_mov_b32_e32 v36, v2
	v_mov_b32_e32 v37, v2
	v_mov_b32_e32 v38, v2
	v_mov_b32_e32 v39, v2
	v_mov_b32_e32 v40, v2
	v_mov_b32_e32 v41, v2
	v_mov_b32_e32 v42, v2
	v_mov_b32_e32 v43, v2
	v_mov_b32_e32 v44, v2
	v_mov_b32_e32 v45, v2
	v_mov_b32_e32 v46, v2
	v_mov_b32_e32 v47, v2
	v_mov_b32_e32 v48, v2
	v_mov_b32_e32 v49, v2
	v_mov_b32_e32 v186, v2
	v_mov_b32_e32 v187, v2
	v_mov_b32_e32 v184, v2
	v_mov_b32_e32 v185, v2
	v_mov_b32_e32 v190, v2
	v_mov_b32_e32 v191, v2
	v_mov_b32_e32 v188, v2
	v_mov_b32_e32 v189, v2

; DI void attn_unit_d8(unsigned char* lds, const AttnArgs& a) {
;     ...
;     const int lane = tid & 63, r = lane & 31, h = lane >> 5; const int wid = __builtin_amdgcn_readfirstlane(tid >> 6);
;     v8i qfa, qfb;
;     { const bf16_t* qp = a.q + (size_t)(wid * 32 + r) * 256 + 32 * h;
;       const u32x4 q0 = *(const u32x4*)qp, q1 = *(const u32x4*)(qp + 8), q2 = *(const u32x4*)(qp + 16), q3 = *(const u32x4*)(qp + 24);
;       const u32x2 c0 = bf8_to_fp8(q0), c1 = bf8_to_fp8(q1), c2 = bf8_to_fp8(q2), c3 = bf8_to_fp8(q3);
;       const v8i qv = (v8i){(int)c0.x, (int)c0.y, (int)c1.x, (int)c1.y, (int)c2.x, (int)c2.y, (int)c3.x, (int)c3.y}, zz = (v8i){0, 0, 0, 0, 0, 0, 0, 0};
;       qfa = h == 0 ? qv : zz; qfb = h == 1 ? qv : zz; }
;     const int lrow = tid >> 3, lch = tid & 7;
;     const unsigned char* vsrc = a.vt8 + (size_t)lrow * KEYS + 8 * lch;
;     const int ldst = lrow * A8_PITCH + lch * 8;
;     const int ldv = A8_VOFF + lrow * A8_PITCH + (lch >> 2) * 16 + (lch & 3) * 4;
;     const int koff = r * A8_PITCH + 32 * h, voff = A8_VOFF + r * A8_PITCH + 32 * h;
;     f32x16 o0[2], o1[2];
; #pragma unroll
;     for (int d = 0; d < 2; ++d) { o0[d] = (f32x16){}; o1[d] = (f32x16){}; }
;     f32x4 l0 = {0.f, 0.f, 0.f, 0.f}, l1 = {0.f, 0.f, 0.f, 0.f};
;     constexpr int D8_SLOT = 2 * 64 * A8_PITCH;
;     u32x2 kreg0, vreg0, kreg1, vreg1;
;     auto gload = [&](int t, u32x2& kreg, u32x2& vreg) __attribute__((always_inline)) {
;         const unsigned char* kp = (t < 64) ? a.klat8 + (size_t)(t * 64 + lrow) * 256 : a.kctx8 + (size_t)((t - 64) * 64 + lrow) * 256;
;         kreg = *(const u32x2*)(kp + 8 * lch);
;         vreg = *(const u32x2*)(vsrc + (size_t)t * 64);
;     };
;     auto lstore = [&](int slot, const u32x2& kreg, const u32x2& vreg) __attribute__((always_inline)) { unsigned char* b = lds + slot * D8_SLOT;
;         *(u32x2*)(b + ldst) = kreg; *(unsigned*)(b + ldv) = vreg.x; *(unsigned*)(b + ldv + 32) = vreg.y; };
;     auto rd32 = [&](const unsigned char* p) __attribute__((always_inline)) -> v8i { const u32x4 lo = *(const u32x4*)p, hi = *(const u32x4*)(p + 16);
;         return (v8i){(int)lo.x, (int)lo.y, (int)lo.z, (int)lo.w, (int)hi.x, (int)hi.y, (int)hi.z, (int)hi.w}; };
;     auto expsum = [&](f32x16& sc, f32x4& l) __attribute__((always_inline)) {
; #pragma unroll
;         for (int i = 0; i < 16; ++i) sc[i] = __builtin_amdgcn_exp2f(sc[i]);
; #pragma unroll
.LBB0_1885:
	s_ashr_i32 s8, s46, 6
	s_lshl_b32 s16, s46, 8
	s_lshl_b32 s18, s8, 12
	s_and_b32 s16, s16, 0xf00
	s_or_b32 s16, s18, s16
	s_ashr_i32 s17, s16, 31
	s_lshl_b64 s[20:21], s[16:17], 9
	s_add_u32 s19, s4, s20
	s_addc_u32 s20, s5, s21
	s_lshl_b32 s21, s46, 2
	s_and_b32 s47, s21, 0xc0
	s_lshl_b32 s21, s47, 1
	s_add_u32 s50, s19, s21
	s_addc_u32 s51, s20, 0
	s_lshl_b32 s20, s8, 8
	s_ashr_i32 s19, s18, 31
	s_or_b32 s8, s20, s47
	s_lshl_b64 s[18:19], s[18:19], 8
	s_mul_hi_i32 s21, s8, 0x1100
	s_mulk_i32 s8, 0x1100
	s_add_u32 s22, s28, s8
	s_addc_u32 s23, s29, s21
	s_add_u32 s8, s24, s18
	s_addc_u32 s19, s25, s19
	v_mov_b32_e32 v18, v0
	s_add_u32 s18, s8, s47
	s_addc_u32 s19, s19, 0
	v_readfirstlane_b32 s8, v18
	v_and_b32_e32 v30, 31, v18
	s_ashr_i32 s8, s8, 6
	v_lshl_or_b32 v180, s8, 5, v30
	v_ashrrev_i32_e32 v181, 31, v180
	v_bfe_u32 v217, v18, 5, 1
	v_lshlrev_b64 v[2:3], 9, v[180:181]
	v_lshl_add_u64 v[2:3], s[50:51], 0, v[2:3]
	v_lshlrev_b32_e32 v178, 6, v217
	v_lshl_add_u64 v[14:15], v[2:3], 0, v[178:179]
	global_load_dwordx4 v[2:5], v[14:15], off
	global_load_dwordx4 v[6:9], v[14:15], off offset:16
	global_load_dwordx4 v[10:13], v[14:15], off offset:32
	s_nop 0
	global_load_dwordx4 v[14:17], v[14:15], off offset:48
	v_ashrrev_i32_e32 v182, 3, v18
	v_ashrrev_i32_e32 v183, 31, v182
	v_bfe_i32 v37, v18, 5, 1
	v_and_b32_e32 v38, 7, v18
	v_lshlrev_b64 v[18:19], 8, v[182:183]
	v_lshl_add_u64 v[18:19], s[18:19], 0, v[18:19]
	v_lshlrev_b32_e32 v178, 3, v38
	v_lshl_add_u64 v[18:19], v[18:19], 0, v[178:179]
	v_mov_b64_e32 v[20:21], s[22:23]
	v_add_co_u32_e32 v22, vcc, s39, v18
	v_mad_i64_i32 v[20:21], s[22:23], v182, s37, v[20:21]
	s_nop 0
	v_addc_co_u32_e32 v23, vcc, 0, v19, vcc
	v_lshl_add_u64 v[184:185], v[20:21], 0, v[178:179]
	global_load_dwordx2 v[20:21], v[18:19], off
	v_add_co_u32_e32 v18, vcc, s40, v18
	s_nop 0
	s_nop 0
	v_addc_co_u32_e32 v19, vcc, 0, v19, vcc
	global_load_dwordx2 v[24:25], v[184:185], off
	global_load_dwordx2 v[26:27], v[184:185], off offset:64
	global_load_dwordx2 v[28:29], v[184:185], off offset:128
	s_nop 0
	global_load_dwordx2 v[22:23], v[22:23], off
	s_nop 0
	global_load_dwordx2 v[18:19], v[18:19], off
	s_nop 0
	s_nop 0
	s_nop 0
	s_nop 0
	s_nop 0
	v_cmp_eq_u32_e32 vcc, 0, v217
	v_lshlrev_b32_e32 v39, 5, v217
	s_cmp_lt_i32 s8, 4
	s_waitcnt vmcnt(9)
	v_lshlrev_b32_e32 v40, 16, v2
	v_and_b32_e32 v2, 0xffff0000, v2
	v_lshlrev_b32_e32 v42, 16, v4
	v_and_b32_e32 v4, 0xffff0000, v4
	v_cvt_pk_fp8_f32 v31, v40, v2
	v_cvt_pk_fp8_f32 v32, v42, v4
	v_lshlrev_b32_e32 v41, 16, v3
	v_and_b32_e32 v3, 0xffff0000, v3
	v_lshlrev_b32_e32 v43, 16, v5
	v_and_b32_e32 v5, 0xffff0000, v5
	s_waitcnt vmcnt(8)
	v_lshlrev_b32_e32 v44, 16, v6
	v_and_b32_e32 v6, 0xffff0000, v6
	v_cvt_pk_fp8_f32 v31, v41, v3 op_sel:[0,0,1]
	s_waitcnt vmcnt(6)
	v_lshlrev_b32_e32 v2, 16, v14
	v_and_b32_e32 v3, 0xffff0000, v14
	s_nop 0
	v_cvt_pk_fp8_f32 v33, v44, v6
	v_cvt_pk_fp8_f32 v32, v43, v5 op_sel:[0,0,1]
	v_cvt_pk_fp8_f32 v4, v2, v3
	v_lshlrev_b32_e32 v3, 16, v16
	v_and_b32_e32 v5, 0xffff0000, v16
	s_nop 0
	v_lshlrev_b32_e32 v46, 16, v8
	v_and_b32_e32 v8, 0xffff0000, v8
	v_lshlrev_b32_e32 v48, 16, v10
	v_and_b32_e32 v10, 0xffff0000, v10
	v_lshlrev_b32_e32 v50, 16, v12
	v_and_b32_e32 v12, 0xffff0000, v12
	v_cvt_pk_fp8_f32 v6, v3, v5
	v_cvt_pk_fp8_f32 v34, v46, v8
	v_cvt_pk_fp8_f32 v35, v48, v10
	v_cvt_pk_fp8_f32 v36, v50, v12
	v_lshlrev_b32_e32 v45, 16, v7
	v_and_b32_e32 v7, 0xffff0000, v7
	v_lshlrev_b32_e32 v2, 16, v15
	v_and_b32_e32 v3, 0xffff0000, v15
	v_cvt_pk_fp8_f32 v33, v45, v7 op_sel:[0,0,1]
	v_lshlrev_b32_e32 v5, 16, v17
	v_and_b32_e32 v7, 0xffff0000, v17
	v_cvt_pk_fp8_f32 v4, v2, v3 op_sel:[0,0,1]
	v_lshlrev_b32_e32 v3, 2, v38
	v_lshlrev_b32_e32 v47, 16, v9
	v_and_b32_e32 v9, 0xffff0000, v9
	v_lshlrev_b32_e32 v49, 16, v11
	v_and_b32_e32 v11, 0xffff0000, v11
	v_lshlrev_b32_e32 v51, 16, v13
	v_and_b32_e32 v13, 0xffff0000, v13
	v_cvt_pk_fp8_f32 v6, v5, v7 op_sel:[0,0,1]
	v_mul_lo_u32 v2, v182, s38
	v_and_b32_e32 v5, 16, v3
	v_cvt_pk_fp8_f32 v34, v47, v9 op_sel:[0,0,1]
	v_cvt_pk_fp8_f32 v35, v49, v11 op_sel:[0,0,1]
	v_cvt_pk_fp8_f32 v36, v51, v13 op_sel:[0,0,1]
	v_add_u32_e32 v183, v2, v178
	v_add_u32_e32 v2, v2, v5
	v_and_or_b32 v218, v3, 12, v2
	v_add_u32_e32 v2, 0, v218
	v_cndmask_b32_e32 v120, 0, v4, vcc
	v_mul_u32_u24_e32 v7, 0x50, v30
	v_and_b32_e32 v128, v37, v4
	v_add_u32_e32 v4, 0, v183
	v_add_u32_e32 v3, 0x1400, v2
	v_cndmask_b32_e32 v121, 0, v6, vcc
	v_cndmask_b32_e32 v119, 0, v36, vcc
	v_cndmask_b32_e32 v118, 0, v35, vcc
	v_cndmask_b32_e32 v117, 0, v34, vcc
	v_cndmask_b32_e32 v116, 0, v33, vcc
	v_cndmask_b32_e32 v115, 0, v32, vcc
	v_cndmask_b32_e32 v114, 0, v31, vcc
	v_and_b32_e32 v129, v37, v6
	v_and_b32_e32 v127, v37, v36
	v_and_b32_e32 v126, v37, v35
	v_and_b32_e32 v125, v37, v34
	v_and_b32_e32 v124, v37, v33
	v_and_b32_e32 v123, v37, v32
	v_and_b32_e32 v122, v37, v31
	s_waitcnt vmcnt(5)
	ds_write_b64 v4, v[20:21]
	s_waitcnt vmcnt(4)
	ds_write2_b32 v3, v24, v25 offset1:8
	s_waitcnt vmcnt(1)
	ds_write_b64 v4, v[22:23] offset:10240
	v_add_u32_e32 v3, 0x3c00, v2
	v_add_u32_e32 v2, 0x6400, v2
	v_add3_u32 v219, v39, v7, 0
	ds_write2_b32 v3, v26, v27 offset1:8
	s_waitcnt vmcnt(0)
	ds_write_b64 v4, v[18:19] offset:20480
	ds_write2_b32 v2, v28, v29 offset1:8
	s_waitcnt lgkmcnt(0)
	s_barrier
	ds_read_b128 v[2:5], v219
	ds_read_b128 v[6:9], v219 offset:16
	s_waitcnt lgkmcnt(0)
	v_mfma_f32_32x32x64_f8f6f4 v[82:97], v[2:9], v[114:121], 0
	v_mfma_f32_32x32x64_f8f6f4 v[66:81], v[2:9], v[122:129], 0
	s_cbranch_scc1 .LBB0_1887
; DI void attn_unit_d8(unsigned char* lds, const AttnArgs& a) {
;     ...
;     f32x16 o0[2], o1[2];
; #pragma unroll
;     for (int d = 0; d < 2; ++d) { o0[d] = (f32x16){}; o1[d] = (f32x16){}; }
;     f32x4 l0 = {0.f, 0.f, 0.f, 0.f}, l1 = {0.f, 0.f, 0.f, 0.f};
;     ...
;     if (wid >= 4) __builtin_amdgcn_s_setprio(1);
;     int sb = 0;
;     const v8i zz8 = (v8i){0, 0, 0, 0, 0, 0, 0, 0};
;     v8i PaX = zz8, PbX = zz8, PaY = zz8, PbY = zz8, vX0 = zz8, vX1 = zz8, vY0 = zz8, vY1 = zz8;
.LBB0_1887:
	s_and_b32 s61, s46, 1
	s_lshl_b32 s61, s61, 3
	s_sub_i32 s61, 0, s61
	s_ashr_i32 s21, s20, 31
	s_lshl_b64 s[20:21], s[20:21], 8
	s_add_u32 s8, s24, s20
	s_addc_u32 s20, s25, s21
	s_add_u32 s8, s8, s47
	s_addc_u32 s21, s20, 0
	s_add_u32 s20, s8, 0x800000
	v_mov_b32_e32 v2, 0
	s_addc_u32 s21, s21, 0
	s_mov_b32 s23, 0
	s_mov_b32 s22, -2
	v_mov_b32_e32 v138, 0
	v_mov_b32_e32 v139, 0
	v_mov_b32_e32 v140, 0
	v_mov_b32_e32 v141, 0
	v_mov_b32_e32 v142, 0
	v_mov_b32_e32 v143, 0
	v_mov_b32_e32 v144, 0
	v_mov_b32_e32 v145, 0
	v_mov_b32_e32 v130, 0
	v_mov_b32_e32 v131, 0
	v_mov_b32_e32 v132, 0
	v_mov_b32_e32 v133, 0
	v_mov_b32_e32 v134, 0
	v_mov_b32_e32 v135, 0
	v_mov_b32_e32 v136, 0
	v_mov_b32_e32 v137, 0
	v_mov_b32_e32 v154, 0
	v_mov_b32_e32 v155, 0
	v_mov_b32_e32 v156, 0
	v_mov_b32_e32 v157, 0
	v_mov_b32_e32 v158, 0
	v_mov_b32_e32 v159, 0
	v_mov_b32_e32 v160, 0
	v_mov_b32_e32 v161, 0
	v_mov_b32_e32 v146, 0
	v_mov_b32_e32 v147, 0
	v_mov_b32_e32 v148, 0
	v_mov_b32_e32 v149, 0
	v_mov_b32_e32 v150, 0
	v_mov_b32_e32 v151, 0
	v_mov_b32_e32 v152, 0
	v_mov_b32_e32 v153, 0
	v_mov_b32_e32 v3, v2
	v_mov_b32_e32 v4, v2
	v_mov_b32_e32 v5, v2
	v_mov_b32_e32 v6, v2
	v_mov_b32_e32 v7, v2
	v_mov_b32_e32 v8, v2
	v_mov_b32_e32 v9, v2
	v_mov_b32_e32 v10, v2
	v_mov_b32_e32 v11, v2
	v_mov_b32_e32 v12, v2
	v_mov_b32_e32 v13, v2
	v_mov_b32_e32 v14, v2
	v_mov_b32_e32 v15, v2
	v_mov_b32_e32 v16, v2
	v_mov_b32_e32 v17, v2
	v_mov_b32_e32 v18, v2
	v_mov_b32_e32 v19, v2
	v_mov_b32_e32 v20, v2
	v_mov_b32_e32 v21, v2
	v_mov_b32_e32 v22, v2
	v_mov_b32_e32 v23, v2
	v_mov_b32_e32 v24, v2
	v_mov_b32_e32 v25, v2
	v_mov_b32_e32 v26, v2
	v_mov_b32_e32 v27, v2
	v_mov_b32_e32 v28, v2
	v_mov_b32_e32 v29, v2
	v_mov_b32_e32 v30, v2
	v_mov_b32_e32 v31, v2
	v_mov_b32_e32 v32, v2
	v_mov_b32_e32 v33, v2
	v_mov_b32_e32 v50, v2
	v_mov_b32_e32 v51, v2
	v_mov_b32_e32 v52, v2
	v_mov_b32_e32 v53, v2
	v_mov_b32_e32 v54, v2
	v_mov_b32_e32 v55, v2
	v_mov_b32_e32 v56, v2
	v_mov_b32_e32 v57, v2
	v_mov_b32_e32 v58, v2
	v_mov_b32_e32 v59, v2
	v_mov_b32_e32 v60, v2
	v_mov_b32_e32 v61, v2
	v_mov_b32_e32 v62, v2
	v_mov_b32_e32 v63, v2
	v_mov_b32_e32 v64, v2
	v_mov_b32_e32 v65, v2
	v_mov_b32_e32 v34, v2
	v_mov_b32_e32 v35, v2
	v_mov_b32_e32 v36, v2
	v_mov_b32_e32 v37, v2
	v_mov_b32_e32 v38, v2
	v_mov_b32_e32 v39, v2
	v_mov_b32_e32 v40, v2
	v_mov_b32_e32 v41, v2
	v_mov_b32_e32 v42, v2
	v_mov_b32_e32 v43, v2
	v_mov_b32_e32 v44, v2
	v_mov_b32_e32 v45, v2
	v_mov_b32_e32 v46, v2
	v_mov_b32_e32 v47, v2
	v_mov_b32_e32 v48, v2
	v_mov_b32_e32 v49, v2
	v_mov_b32_e32 v188, v2
	v_mov_b32_e32 v189, v2
	v_mov_b32_e32 v186, v2
	v_mov_b32_e32 v187, v2
	v_mov_b32_e32 v192, v2
	v_mov_b32_e32 v193, v2
	v_mov_b32_e32 v190, v2
	v_mov_b32_e32 v191, v2
